# baseline (speedup 1.0000x reference)
.LBB0_19:
	s_and_b64 vcc, exec, s[2:3]
	s_cbranch_vccz .LBB0_114
	s_load_dwordx2 s[4:5], s[0:1], 0x40
	s_load_dwordx2 s[8:9], s[0:1], 0x0
	v_lshl_or_b32 v2, s26, 10, v0
	v_add_u32_e32 v7, 0xfff9e400, v2
	v_lshlrev_b32_e32 v2, 5, v7
	v_mul_u32_u24_e32 v6, 0xc350, v1
	v_lshlrev_b32_e32 v1, 4, v0
	v_and_b32_e32 v1, 0x70, v1
	v_lshrrev_b32_e32 v16, 5, v7
	v_add_u32_e32 v16, v16, v6
	v_lshl_or_b32 v40, v16, 7, v1
	s_mov_b32 s7, 0x20000
	s_mov_b32 s6, 0x186a000
	v_add_u32_e32 v3, 0x2000, v2
	v_add_u32_e32 v4, 0x4000, v2
	v_add_u32_e32 v5, 0x6000, v2
	s_waitcnt lgkmcnt(0)
	s_and_b32 s5, s5, 0xffff
	global_load_dwordx4 v[8:11], v2, s[8:9] nt
	global_load_dwordx4 v[12:15], v2, s[8:9] offset:16 nt
	global_load_dwordx4 v[16:19], v3, s[8:9] nt
	global_load_dwordx4 v[20:23], v3, s[8:9] offset:16 nt
	s_cmpk_eq_i32 s26, 0x7a1
	s_cbranch_scc1 .Lconv_last
	s_waitcnt vmcnt(2)
	v_cvt_pk_f16_f32 v8, v8, v9
	v_cvt_pk_f16_f32 v9, v10, v11
	v_cvt_pk_f16_f32 v10, v12, v13
	v_cvt_pk_f16_f32 v11, v14, v15
	buffer_store_dwordx4 v[8:11], v40, s[4:7], 0 offen sc1
	global_load_dwordx4 v[24:27], v4, s[8:9] nt
	global_load_dwordx4 v[28:31], v4, s[8:9] offset:16 nt
	s_waitcnt vmcnt(3)
	v_cvt_pk_f16_f32 v16, v16, v17
	v_cvt_pk_f16_f32 v17, v18, v19
	v_cvt_pk_f16_f32 v18, v20, v21
	v_cvt_pk_f16_f32 v19, v22, v23
	buffer_store_dwordx4 v[16:19], v40, s[4:7], 0 offen offset:1024 sc1
	global_load_dwordx4 v[32:35], v5, s[8:9] nt
	global_load_dwordx4 v[36:39], v5, s[8:9] offset:16 nt
	s_waitcnt vmcnt(3)
	v_cvt_pk_f16_f32 v24, v24, v25
	v_cvt_pk_f16_f32 v25, v26, v27
	v_cvt_pk_f16_f32 v26, v28, v29
	v_cvt_pk_f16_f32 v27, v30, v31
	buffer_store_dwordx4 v[24:27], v40, s[4:7], 0 offen offset:2048 sc1
	s_waitcnt vmcnt(1)
	v_cvt_pk_f16_f32 v32, v32, v33
	v_cvt_pk_f16_f32 v33, v34, v35
	v_cvt_pk_f16_f32 v34, v36, v37
	v_cvt_pk_f16_f32 v35, v38, v39
	buffer_store_dwordx4 v[32:35], v40, s[4:7], 0 offen offset:3072 sc1
	s_branch .LBB0_115
.Lconv_last:
	s_waitcnt vmcnt(2)
	v_cvt_pk_f16_f32 v8, v8, v9
	v_cvt_pk_f16_f32 v9, v10, v11
	v_cvt_pk_f16_f32 v10, v12, v13
	v_cvt_pk_f16_f32 v11, v14, v15
	buffer_store_dwordx4 v[8:11], v40, s[4:7], 0 offen sc1
	s_waitcnt vmcnt(1)
	v_cvt_pk_f16_f32 v16, v16, v17
	v_cvt_pk_f16_f32 v17, v18, v19
	v_cvt_pk_f16_f32 v18, v20, v21
	v_cvt_pk_f16_f32 v19, v22, v23
	buffer_store_dwordx4 v[16:19], v40, s[4:7], 0 offen offset:1024 sc1
	s_branch .LBB0_115
